# baseline (speedup 1.0000x reference)
.LBB2_11:
	v_and_b32_e32 v28, 8, v0
	v_lshlrev_b32_e32 v0, 1, v5
	v_lshl_or_b32 v38, v6, 4, v0
	v_lshlrev_b32_e32 v0, 7, v1
	v_mov_b32_e32 v29, 0xeeeeeeee
	v_mov_b32_e32 v30, 0x44444444
	v_cmp_eq_u32_e32 vcc, 0, v28
	v_lshl_add_u64 v[2:3], s[20:21], 0, v[2:3]
	v_lshl_or_b32 v40, s24, 9, v0
	v_cndmask_b32_e64 v0, 0, 1, s[0:1]
	v_cndmask_b32_e32 v28, v29, v30, vcc
	s_waitcnt vmcnt(9)
	v_and_b32_e32 v44, 0xffff, v8
	s_waitcnt vmcnt(8)
	v_and_b32_e32 v43, 0xffff, v9
	s_waitcnt vmcnt(7)
	v_and_b32_e32 v42, 0xffff, v11
	s_waitcnt vmcnt(3)
	v_and_b32_e32 v41, 0xffff, v24
	v_and_b32_e32 v29, 0xffff, v10
	v_and_b32_e32 v30, 0xffff, v12
	s_waitcnt vmcnt(2)
	v_and_b32_e32 v31, 0xffff, v13
	s_waitcnt vmcnt(1)
	v_and_b32_e32 v32, 0xffff, v15
	v_and_b32_e32 v45, 0xffff, v14
	s_waitcnt vmcnt(0)
	v_and_b32_e32 v33, 0xffff, v25
	s_mov_b32 s19, 0x20000
	s_mov_b32 s18, 0x40000
	s_and_b32 s17, s9, 0xffff
	s_mov_b32 s16, s8
	v_lshl_add_u64 v[24:25], v[16:17], 2, v[2:3]
	v_lshlrev_b32_e32 v35, 9, v4
	v_lshlrev_b32_e32 v36, 7, v7
	v_lshlrev_b32_e32 v37, 4, v5
	v_cmp_eq_u32_e64 s[2:3], 0, v4
	v_lshl_add_u32 v34, v1, 10, v35
	v_add3_u32 v34, v34, v36, v37
	v_add_u32_e32 v121, 1, v1
	v_add_u32_e32 v122, 2, v1
	v_add_u32_e32 v123, 3, v1
	v_and_b32_e32 v121, 3, v121
	v_and_b32_e32 v122, 3, v122
	v_and_b32_e32 v123, 3, v123
	v_lshl_add_u32 v121, v121, 10, v35
	v_lshl_add_u32 v122, v122, 10, v35
	v_lshl_add_u32 v123, v123, 10, v35
	v_add3_u32 v121, v121, v36, v37
	v_add3_u32 v122, v122, v36, v37
	v_add3_u32 v123, v123, v36, v37
	v_lshl_or_b32 v39, v27, 14, v34
	s_mov_b64 s[6:7], 0
	s_mov_b32 s28, 0x10000
	v_cmp_ne_u32_e64 s[0:1], 1, v0
	v_mov_b32_e32 v46, 0
	s_mov_b32 s29, 0
	v_lshl_add_u32 v120, v27, 14, v40
	v_or_b32_e32 v120, v120, v38
	s_mov_b32 s37, 0
	s_mov_b32 s40, 0xbfb8aa3b
	s_mov_b32 s41, 0xbfb8aa3b
	s_mov_b32 s42, 0x4038aa3b
	s_mov_b32 s43, 0xbfb8aa3b
	s_mov_b32 s44, 1.0
	s_mov_b32 s45, 1.0
	s_cmp_eq_u32 s29, 0
	s_cbranch_scc1 .LBB2_23

.LBB2_20:
	s_mov_b64 exec, -1
	s_waitcnt lgkmcnt(0)
	s_barrier
	ds_read_b128 v[50:53], v111
	ds_read_b128 v[54:57], v111 offset:4096
	ds_read_b128 v[58:61], v111 offset:8192
	ds_read_b128 v[70:73], v111 offset:12288
	ds_read_b128 v[78:81], v124
	ds_read_b128 v[82:85], v124 offset:4096
	ds_read_b128 v[86:89], v124 offset:8192
	ds_read_b128 v[90:93], v124 offset:12288
	ds_read_b128 v[94:97], v125
	ds_read_b128 v[98:101], v125 offset:4096
	ds_read_b128 v[102:105], v125 offset:8192
	ds_read_b128 v[106:109], v125 offset:12288
	v_smfmac_f32_16x16x64_f16 v[62:65], v[0:3], a[0:7], v28
	v_smfmac_f32_16x16x64_f16 v[66:69], v[0:3], a[128:135], v28
	v_mov_b32_e32 v29, v128
	v_mov_b32_e32 v30, v129
	v_mov_b32_e32 v31, v130
	v_mov_b32_e32 v32, v131
	v_mov_b32_e32 v33, v132
	v_smfmac_f32_16x16x64_f16 v[62:65], v[4:7], a[8:15], v28
	v_smfmac_f32_16x16x64_f16 v[66:69], v[4:7], a[136:143], v28
	global_load_ushort v128, v[114:115], off
	v_smfmac_f32_16x16x64_f16 v[62:65], v[8:11], a[16:23], v28
	v_smfmac_f32_16x16x64_f16 v[66:69], v[8:11], a[144:151], v28
	global_load_ushort v129, v[114:115], off offset:2048
	v_smfmac_f32_16x16x64_f16 v[62:65], v[12:15], a[24:31], v28
	v_smfmac_f32_16x16x64_f16 v[66:69], v[12:15], a[152:159], v28
	global_load_ushort v130, v[116:117], off
	s_waitcnt lgkmcnt(11)
	v_smfmac_f32_16x16x64_f16 v[62:65], v[50:53], a[32:39], v28
	v_smfmac_f32_16x16x64_f16 v[66:69], v[50:53], a[160:167], v28
	global_load_ushort v131, v[116:117], off offset:2048
	s_waitcnt lgkmcnt(10)
	v_smfmac_f32_16x16x64_f16 v[62:65], v[54:57], a[40:47], v28
	v_smfmac_f32_16x16x64_f16 v[66:69], v[54:57], a[168:175], v28
	global_load_ushort v132, v[118:119], off
	s_waitcnt lgkmcnt(9)
	v_smfmac_f32_16x16x64_f16 v[62:65], v[58:61], a[48:55], v28
	v_smfmac_f32_16x16x64_f16 v[66:69], v[58:61], a[176:183], v28
	global_store_dword v[112:113], v46, off
	s_waitcnt lgkmcnt(8)
	v_smfmac_f32_16x16x64_f16 v[62:65], v[70:73], a[56:63], v28
	v_smfmac_f32_16x16x64_f16 v[66:69], v[70:73], a[184:191], v28
	v_cvt_f32_f16_e32 v112, v44
	v_cvt_f32_f16_e32 v113, v43
	v_cvt_f32_f16_e32 v114, v42
	v_cvt_f32_f16_e32 v115, v41
	v_cvt_f32_f16_e32 v118, v45
	v_cndmask_b32_e64 v116, 0, v118, s[22:23]
	v_cndmask_b32_e64 v117, v118, 0, s[22:23]
	v_add_f32_e32 v113, v113, v116
	v_add_f32_e32 v115, v115, v117
	s_waitcnt lgkmcnt(7)
	v_smfmac_f32_16x16x64_f16 v[62:65], v[78:81], a[64:71], v28
	v_smfmac_f32_16x16x64_f16 v[66:69], v[78:81], a[192:199], v28
	s_waitcnt lgkmcnt(6)
	v_smfmac_f32_16x16x64_f16 v[62:65], v[82:85], a[72:79], v28
	v_smfmac_f32_16x16x64_f16 v[66:69], v[82:85], a[200:207], v28
	s_waitcnt lgkmcnt(5)
	v_smfmac_f32_16x16x64_f16 v[62:65], v[86:89], a[80:87], v28
	v_smfmac_f32_16x16x64_f16 v[66:69], v[86:89], a[208:215], v28
	s_waitcnt lgkmcnt(4)
	v_smfmac_f32_16x16x64_f16 v[62:65], v[90:93], a[88:95], v28
	v_smfmac_f32_16x16x64_f16 v[66:69], v[90:93], a[216:223], v28
	s_waitcnt lgkmcnt(3)
	v_smfmac_f32_16x16x64_f16 v[62:65], v[94:97], a[96:103], v28
	v_smfmac_f32_16x16x64_f16 v[66:69], v[94:97], a[224:231], v28
	s_waitcnt lgkmcnt(2)
	v_smfmac_f32_16x16x64_f16 v[62:65], v[98:101], a[104:111], v28
	v_smfmac_f32_16x16x64_f16 v[66:69], v[98:101], a[232:239], v28
	s_waitcnt lgkmcnt(1)
	v_smfmac_f32_16x16x64_f16 v[62:65], v[102:105], a[112:119], v28
	v_smfmac_f32_16x16x64_f16 v[66:69], v[102:105], a[240:247], v28
	s_waitcnt lgkmcnt(0)
	v_smfmac_f32_16x16x64_f16 v[62:65], v[106:109], a[120:127], v28
	v_smfmac_f32_16x16x64_f16 v[66:69], v[106:109], a[248:255], v28
	s_nop 6
	v_permlane32_swap_b32_e32 v62, v63
	v_permlane32_swap_b32_e32 v64, v65
	v_permlane32_swap_b32_e32 v66, v67
	v_permlane32_swap_b32_e32 v68, v69
	v_add_f32_e32 v2, v62, v63
	v_add_f32_e32 v3, v64, v65
	v_add_f32_e32 v6, v66, v67
	v_add_f32_e32 v7, v68, v69
.Lrec_gate2:
	v_cndmask_b32_e64 v4, v2, v3, s[2:3]
	v_cndmask_b32_e64 v5, v6, v7, s[2:3]
	s_nop 0
	v_mov_b32_dpp v2, v4 row_ror:8 row_mask:0xf bank_mask:0xc
	v_mov_b32_dpp v3, v4 row_ror:8 row_mask:0xf bank_mask:0x3
	v_mov_b32_dpp v6, v5 row_ror:8 row_mask:0xf bank_mask:0xc
	v_mov_b32_dpp v7, v5 row_ror:8 row_mask:0xf bank_mask:0x3
	v_pk_add_f32 v[2:3], v[2:3], v[112:113]
	v_pk_add_f32 v[6:7], v[6:7], v[114:115]
	v_pk_mul_f32 v[2:3], v[2:3], s[40:41]
	v_pk_mul_f32 v[6:7], v[6:7], s[42:43]
	v_exp_f32_e32 v2, v2
	v_exp_f32_e32 v6, v6
	v_exp_f32_e32 v3, v3
	v_exp_f32_e32 v7, v7
	s_nop 0
	v_pk_add_f32 v[2:3], v[2:3], s[44:45]
	v_pk_add_f32 v[6:7], v[6:7], s[44:45]
	v_rcp_f32_e32 v6, v6
	v_rcp_f32_e32 v2, v2
	v_rcp_f32_e32 v3, v3
	v_rcp_f32_e32 v7, v7
	v_fma_f32 v0, v6, -2.0, 1.0
	v_mul_f32_e32 v0, v2, v0
	v_fmac_f32_e32 v0, v26, v3
	v_mul_f32_e32 v1, 0x4038aa3b, v0
	v_exp_f32_e32 v1, v1
	s_cmpk_eq_i32 s29, 0x7f
	v_add_f32_e32 v1, 1.0, v1
	v_rcp_f32_e32 v1, v1
	s_nop 0
	v_fma_f32 v1, v1, -2.0, 1.0
	v_mul_f32_e32 v46, v7, v1
	s_cbranch_scc1 .LBB2_29
	v_cvt_f16_f32_e32 v2, v46
	s_cmp_lg_u64 s[0:1], 0
	v_bitop3_b16 v2, s37, v2, -2 bitop3:0xf8
	s_cbranch_scc1 .Lrec_pub_slow
	global_store_short v120, v2, s[8:9]
	s_branch .LBB2_29

.LBB2_23:
	s_mov_b32 s32, 0x4000
	s_mov_b32 s33, 0
	v_lshl_add_u64 v[114:115], v[20:21], 0, s[32:33]
	v_lshl_add_u64 v[118:119], v[22:23], 0, s[32:33]
	v_add_co_u32_e32 v116, vcc, 0x1000, v114
	s_nop 1
	v_addc_co_u32_e32 v117, vcc, 0, v115, vcc
	global_load_ushort v128, v[114:115], off
	global_load_ushort v129, v[114:115], off offset:2048
	global_load_ushort v130, v[116:117], off
	global_load_ushort v131, v[116:117], off offset:2048
	global_load_ushort v132, v[118:119], off
	v_mov_b32_e32 v2, 0
	v_mov_b32_e32 v3, 0
	v_mov_b32_e32 v6, 0
	v_mov_b32_e32 v7, 0
	v_cvt_f32_f16_e32 v112, v44
	v_cvt_f32_f16_e32 v113, v43
	v_cvt_f32_f16_e32 v114, v42
	v_cvt_f32_f16_e32 v115, v41
	v_cvt_f32_f16_e32 v118, v45
	v_cndmask_b32_e64 v116, 0, v118, s[22:23]
	v_cndmask_b32_e64 v117, v118, 0, s[22:23]
	v_add_f32_e32 v113, v113, v116
	v_add_f32_e32 v115, v115, v117
	s_branch .Lrec_gate2
